# baseline (speedup 1.0000x reference)
.LBB3_13:
	s_or_b64 exec, exec, s[4:5]
	v_mov_b32_e32 v172, 0
	v_ashrrev_i32_e32 v1, 2, v0
	v_and_b32_e32 v1, 0xffffffc0, v1
	v_add_u32_e32 v1, s8, v1
	v_lshrrev_b32_e32 v130, 2, v0
	v_and_or_b32 v156, v130, 12, v1
	v_ashrrev_i32_e32 v157, 31, v156
	v_lshl_add_u64 v[150:151], v[156:157], 2, s[2:3]
	global_load_dwordx4 v[138:141], v[150:151], off
	global_load_dwordx4 v[142:145], v[150:151], off offset:64
	v_and_b32_e32 v130, 15, v0
	v_and_b32_e32 v180, 1, v0
	v_lshrrev_b32_e32 v0, 1, v0
	v_and_b32_e32 v131, 0x60, v0
	s_movk_i32 s3, 0xff6e
	v_lshl_or_b32 v131, s33, 8, v131
	v_lshlrev_b32_e32 v0, 4, v180
	v_or_b32_e32 v181, v131, v130
	v_bitop3_b32 v158, v131, s3, v130 bitop3:0xc8
	v_or_b32_e32 v130, v0, v156
	v_or_b32_e32 v132, 1, v181
	v_or_b32_e32 v134, 16, v158
	v_or_b32_e32 v136, 17, v181
	v_ashrrev_i32_e32 v131, 31, v130
	v_ashrrev_i32_e32 v133, 31, v132
	v_ashrrev_i32_e32 v135, 31, v134
	v_ashrrev_i32_e32 v137, 31, v136
	v_lshl_add_u64 v[160:161], v[130:131], 2, s[0:1]
	v_lshlrev_b64 v[152:153], 12, v[132:133]
	v_lshlrev_b64 v[148:149], 12, v[134:135]
	v_lshlrev_b64 v[146:147], 12, v[136:137]
	global_load_dwordx4 v[130:133], v[150:151], off offset:128
	global_load_dwordx4 v[134:137], v[150:151], off offset:192
	global_load_dwordx4 v[184:187], v[150:151], off offset:576
	global_load_dwordx4 v[188:191], v[150:151], off offset:512
	global_load_dwordx4 v[192:195], v[150:151], off offset:640
	global_load_dwordx4 v[196:199], v[150:151], off offset:704
	s_mov_b32 s2, 0x34800000
	v_cmp_eq_u32_e32 vcc, 0, v180
	v_mov_b32_e32 v173, 0
	v_mov_b32_e32 v174, 0
	v_mov_b32_e32 v175, 0
	v_ashrrev_i32_e32 v159, 31, v158
	v_mov_b32_e32 v176, 0
	v_mov_b32_e32 v177, 0
	v_mov_b32_e32 v178, 0
	v_mov_b32_e32 v179, 0
	v_lshlrev_b64 v[154:155], 12, v[158:159]
	v_lshl_add_u64 v[162:163], v[160:161], 0, v[154:155]
	v_lshl_add_u64 v[164:165], v[160:161], 0, v[152:153]
	v_lshl_add_u64 v[166:167], v[160:161], 0, v[148:149]
	v_mov_b32_e32 v1, 0
	s_waitcnt vmcnt(0)
	v_pk_fma_f32 v[128:129], v[128:129], s[2:3], v[140:141] op_sel_hi:[1,0,1]
	v_pk_fma_f32 v[126:127], v[126:127], s[2:3], v[138:139] op_sel_hi:[1,0,1]
	v_pk_fma_f32 v[120:121], v[120:121], s[2:3], v[144:145] op_sel_hi:[1,0,1]
	v_pk_fma_f32 v[118:119], v[118:119], s[2:3], v[142:143] op_sel_hi:[1,0,1]
	v_pk_fma_f32 v[124:125], v[124:125], s[2:3], v[140:141] op_sel_hi:[1,0,1]
	v_pk_fma_f32 v[122:123], v[122:123], s[2:3], v[138:139] op_sel_hi:[1,0,1]
	v_pk_fma_f32 v[168:169], v[116:117], s[2:3], v[144:145] op_sel_hi:[1,0,1]
	v_pk_fma_f32 v[170:171], v[114:115], s[2:3], v[142:143] op_sel_hi:[1,0,1]
	v_cndmask_b32_e32 v114, v129, v121, vcc
	v_cndmask_b32_e32 v115, v128, v120, vcc
	v_cndmask_b32_e32 v116, v127, v119, vcc
	v_cndmask_b32_e32 v117, v126, v118, vcc
	v_cndmask_b32_e32 v159, v125, v169, vcc
	v_cndmask_b32_e32 v180, v124, v168, vcc
	v_cndmask_b32_e32 v182, v123, v171, vcc
	v_cndmask_b32_e32 v183, v122, v170, vcc
	v_mov_b32_dpp v172, v117 quad_perm:[1,0,3,2] row_mask:0xf bank_mask:0xf
	v_mov_b32_dpp v173, v116 quad_perm:[1,0,3,2] row_mask:0xf bank_mask:0xf
	v_mov_b32_dpp v174, v115 quad_perm:[1,0,3,2] row_mask:0xf bank_mask:0xf
	v_mov_b32_dpp v175, v114 quad_perm:[1,0,3,2] row_mask:0xf bank_mask:0xf
	v_mov_b32_dpp v176, v183 quad_perm:[1,0,3,2] row_mask:0xf bank_mask:0xf
	v_mov_b32_dpp v177, v182 quad_perm:[1,0,3,2] row_mask:0xf bank_mask:0xf
	v_mov_b32_dpp v178, v180 quad_perm:[1,0,3,2] row_mask:0xf bank_mask:0xf
	v_mov_b32_dpp v179, v159 quad_perm:[1,0,3,2] row_mask:0xf bank_mask:0xf
	v_cndmask_b32_e32 v117, v175, v129, vcc
	v_cndmask_b32_e32 v116, v174, v128, vcc
	v_cndmask_b32_e32 v115, v173, v127, vcc
	v_cndmask_b32_e32 v114, v172, v126, vcc
	v_cndmask_b32_e32 v119, v119, v173, vcc
	v_pk_fma_f32 v[110:111], v[110:111], s[2:3], v[138:139] op_sel_hi:[1,0,1]
	v_pk_fma_f32 v[106:107], v[106:107], s[2:3], v[142:143] op_sel_hi:[1,0,1]
	v_cndmask_b32_e32 v121, v121, v175, vcc
	v_cndmask_b32_e32 v120, v120, v174, vcc
	v_cndmask_b32_e32 v118, v118, v172, vcc
	v_cndmask_b32_e32 v125, v179, v125, vcc
	v_cndmask_b32_e32 v124, v178, v124, vcc
	v_cndmask_b32_e32 v123, v177, v123, vcc
	v_cndmask_b32_e32 v122, v176, v122, vcc
	v_cndmask_b32_e32 v129, v169, v179, vcc
	v_cndmask_b32_e32 v128, v168, v178, vcc
	v_cndmask_b32_e32 v127, v171, v177, vcc
	v_cndmask_b32_e32 v126, v170, v176, vcc
	global_store_dwordx4 v[162:163], v[114:117], off
	global_store_dwordx4 v[164:165], v[118:121], off
	global_store_dwordx4 v[166:167], v[122:125], off
	v_lshl_add_u64 v[114:115], v[160:161], 0, v[146:147]
	v_pk_fma_f32 v[112:113], v[112:113], s[2:3], v[140:141] op_sel_hi:[1,0,1]
	v_pk_fma_f32 v[108:109], v[108:109], s[2:3], v[144:145] op_sel_hi:[1,0,1]
	v_cndmask_b32_e32 v116, v111, v107, vcc
	v_mov_b32_e32 v119, 0
	global_store_dwordx4 v[114:115], v[126:129], off
	v_cndmask_b32_e32 v115, v112, v108, vcc
	v_cndmask_b32_e32 v117, v110, v106, vcc
	v_mov_b32_e32 v118, 0
	v_mov_b32_dpp v119, v116 quad_perm:[1,0,3,2] row_mask:0xf bank_mask:0xf
	v_mov_b32_e32 v116, 0
	v_cndmask_b32_e32 v114, v113, v109, vcc
	v_mov_b32_dpp v118, v117 quad_perm:[1,0,3,2] row_mask:0xf bank_mask:0xf
	v_mov_b32_dpp v116, v115 quad_perm:[1,0,3,2] row_mask:0xf bank_mask:0xf
	v_mov_b32_e32 v115, 0
	v_cndmask_b32_e32 v112, v116, v112, vcc
	v_cndmask_b32_e32 v116, v108, v116, vcc
	v_mov_b32_dpp v115, v114 quad_perm:[1,0,3,2] row_mask:0xf bank_mask:0xf
	v_cndmask_b32_e32 v114, v106, v118, vcc
	v_or_b32_e32 v106, 0x80, v158
	v_cndmask_b32_e32 v113, v115, v113, vcc
	v_cndmask_b32_e32 v117, v109, v115, vcc
	v_cndmask_b32_e32 v115, v107, v119, vcc
	v_ashrrev_i32_e32 v107, 31, v106
	v_lshlrev_b64 v[108:109], 12, v[106:107]
	v_cndmask_b32_e32 v111, v119, v111, vcc
	v_cndmask_b32_e32 v110, v118, v110, vcc
	v_lshl_add_u64 v[106:107], v[160:161], 0, v[108:109]
	global_store_dwordx4 v[106:107], v[110:113], off
	v_or_b32_e32 v106, 0x81, v181
	v_ashrrev_i32_e32 v107, 31, v106
	v_lshlrev_b64 v[106:107], 12, v[106:107]
	v_lshl_add_u64 v[110:111], v[160:161], 0, v[106:107]
	v_pk_fma_f32 v[102:103], v[102:103], s[2:3], v[138:139] op_sel_hi:[1,0,1]
	v_pk_fma_f32 v[98:99], v[98:99], s[2:3], v[142:143] op_sel_hi:[1,0,1]
	global_store_dwordx4 v[110:111], v[114:117], off
	v_pk_fma_f32 v[104:105], v[104:105], s[2:3], v[140:141] op_sel_hi:[1,0,1]
	v_pk_fma_f32 v[100:101], v[100:101], s[2:3], v[144:145] op_sel_hi:[1,0,1]
	v_cndmask_b32_e32 v112, v103, v99, vcc
	v_mov_b32_e32 v115, 0
	v_cndmask_b32_e32 v111, v104, v100, vcc
	v_cndmask_b32_e32 v113, v102, v98, vcc
	v_mov_b32_e32 v114, 0
	v_mov_b32_dpp v115, v112 quad_perm:[1,0,3,2] row_mask:0xf bank_mask:0xf
	v_mov_b32_e32 v112, 0
	v_cndmask_b32_e32 v110, v105, v101, vcc
	v_mov_b32_dpp v114, v113 quad_perm:[1,0,3,2] row_mask:0xf bank_mask:0xf
	v_mov_b32_dpp v112, v111 quad_perm:[1,0,3,2] row_mask:0xf bank_mask:0xf
	v_mov_b32_e32 v111, 0
	v_cndmask_b32_e32 v104, v112, v104, vcc
	v_cndmask_b32_e32 v112, v100, v112, vcc
	v_mov_b32_dpp v111, v110 quad_perm:[1,0,3,2] row_mask:0xf bank_mask:0xf
	v_cndmask_b32_e32 v110, v98, v114, vcc
	v_or_b32_e32 v98, 0x90, v158
	v_cndmask_b32_e32 v105, v111, v105, vcc
	v_cndmask_b32_e32 v113, v101, v111, vcc
	v_cndmask_b32_e32 v111, v99, v115, vcc
	v_ashrrev_i32_e32 v99, 31, v98
	v_lshlrev_b64 v[100:101], 12, v[98:99]
	v_cndmask_b32_e32 v103, v115, v103, vcc
	v_cndmask_b32_e32 v102, v114, v102, vcc
	v_lshl_add_u64 v[98:99], v[160:161], 0, v[100:101]
	global_store_dwordx4 v[98:99], v[102:105], off
	v_or_b32_e32 v98, 0x91, v181
	v_ashrrev_i32_e32 v99, 31, v98
	v_lshlrev_b64 v[98:99], 12, v[98:99]
	v_lshl_add_u64 v[102:103], v[160:161], 0, v[98:99]
	global_store_dwordx4 v[102:103], v[110:113], off
	v_pk_fma_f32 v[96:97], v[96:97], s[2:3], v[132:133] op_sel_hi:[1,0,1]
	v_pk_fma_f32 v[94:95], v[94:95], s[2:3], v[130:131] op_sel_hi:[1,0,1]
	v_pk_fma_f32 v[104:105], v[92:93], s[2:3], v[136:137] op_sel_hi:[1,0,1]
	v_pk_fma_f32 v[110:111], v[90:91], s[2:3], v[134:135] op_sel_hi:[1,0,1]
	v_lshl_add_u64 v[102:103], v[0:1], 0, v[156:157]
	v_cndmask_b32_e32 v90, v97, v105, vcc
	v_cndmask_b32_e32 v91, v96, v104, vcc
	v_cndmask_b32_e32 v92, v95, v111, vcc
	v_cndmask_b32_e32 v93, v94, v110, vcc
	v_mov_b32_e32 v112, v1
	v_mov_b32_e32 v113, v1
	v_mov_b32_e32 v114, v1
	v_mov_b32_e32 v115, v1
	v_lshl_add_u64 v[102:103], v[102:103], 2, s[0:1]
	v_mov_b32_dpp v112, v93 quad_perm:[1,0,3,2] row_mask:0xf bank_mask:0xf
	v_mov_b32_dpp v113, v92 quad_perm:[1,0,3,2] row_mask:0xf bank_mask:0xf
	v_mov_b32_dpp v114, v91 quad_perm:[1,0,3,2] row_mask:0xf bank_mask:0xf
	v_mov_b32_dpp v115, v90 quad_perm:[1,0,3,2] row_mask:0xf bank_mask:0xf
	v_cndmask_b32_e32 v93, v115, v97, vcc
	v_cndmask_b32_e32 v92, v114, v96, vcc
	v_cndmask_b32_e32 v91, v113, v95, vcc
	v_cndmask_b32_e32 v90, v112, v94, vcc
	v_cndmask_b32_e32 v97, v105, v115, vcc
	v_cndmask_b32_e32 v96, v104, v114, vcc
	v_lshl_add_u64 v[104:105], v[102:103], 0, v[154:155]
	v_cndmask_b32_e32 v95, v111, v113, vcc
	v_cndmask_b32_e32 v94, v110, v112, vcc
	global_store_dwordx4 v[104:105], v[90:93], off offset:128
	v_pk_fma_f32 v[104:105], v[82:83], s[2:3], v[134:135] op_sel_hi:[1,0,1]
	v_mov_b32_e32 v111, v1
	v_lshl_add_u64 v[90:91], v[102:103], 0, v[152:153]
	global_store_dwordx4 v[90:91], v[94:97], off offset:128
	v_pk_fma_f32 v[90:91], v[88:89], s[2:3], v[132:133] op_sel_hi:[1,0,1]
	v_mov_b32_e32 v112, v1
	v_pk_fma_f32 v[94:95], v[86:87], s[2:3], v[130:131] op_sel_hi:[1,0,1]
	v_pk_fma_f32 v[96:97], v[84:85], s[2:3], v[136:137] op_sel_hi:[1,0,1]
	v_cndmask_b32_e32 v82, v94, v104, vcc
	s_nop 0
	v_cndmask_b32_e32 v110, v95, v105, vcc
	v_mov_b32_dpp v111, v82 quad_perm:[1,0,3,2] row_mask:0xf bank_mask:0xf
	s_nop 0
	v_cndmask_b32_e32 v92, v91, v97, vcc
	v_cndmask_b32_e32 v93, v90, v96, vcc
	v_mov_b32_dpp v112, v110 quad_perm:[1,0,3,2] row_mask:0xf bank_mask:0xf
	v_mov_b32_e32 v110, v1
	v_mov_b32_e32 v113, v1
	v_pk_fma_f32 v[80:81], v[80:81], s[2:3], v[132:133] op_sel_hi:[1,0,1]
	v_mov_b32_dpp v110, v93 quad_perm:[1,0,3,2] row_mask:0xf bank_mask:0xf
	v_mov_b32_dpp v113, v92 quad_perm:[1,0,3,2] row_mask:0xf bank_mask:0xf
	v_cndmask_b32_e32 v93, v113, v91, vcc
	v_cndmask_b32_e32 v92, v110, v90, vcc
	v_cndmask_b32_e32 v91, v112, v95, vcc
	v_cndmask_b32_e32 v90, v111, v94, vcc
	v_cndmask_b32_e32 v95, v105, v112, vcc
	v_cndmask_b32_e32 v94, v104, v111, vcc
	v_lshl_add_u64 v[104:105], v[102:103], 0, v[148:149]
	v_cndmask_b32_e32 v97, v97, v113, vcc
	v_cndmask_b32_e32 v96, v96, v110, vcc
	global_store_dwordx4 v[104:105], v[90:93], off offset:128
	v_pk_fma_f32 v[78:79], v[78:79], s[2:3], v[130:131] op_sel_hi:[1,0,1]
	v_pk_fma_f32 v[72:73], v[72:73], s[2:3], v[132:133] op_sel_hi:[1,0,1]
	v_lshl_add_u64 v[90:91], v[102:103], 0, v[146:147]
	global_store_dwordx4 v[90:91], v[94:97], off offset:128
	v_pk_fma_f32 v[90:91], v[76:77], s[2:3], v[136:137] op_sel_hi:[1,0,1]
	v_pk_fma_f32 v[92:93], v[74:75], s[2:3], v[134:135] op_sel_hi:[1,0,1]
	v_cndmask_b32_e32 v74, v81, v91, vcc
	v_cndmask_b32_e32 v75, v80, v90, vcc
	v_cndmask_b32_e32 v76, v79, v93, vcc
	v_cndmask_b32_e32 v77, v78, v92, vcc
	v_mov_b32_e32 v94, v1
	v_mov_b32_e32 v95, v1
	v_mov_b32_e32 v96, v1
	v_mov_b32_e32 v97, v1
	v_mov_b32_dpp v94, v77 quad_perm:[1,0,3,2] row_mask:0xf bank_mask:0xf
	v_mov_b32_dpp v95, v76 quad_perm:[1,0,3,2] row_mask:0xf bank_mask:0xf
	v_mov_b32_dpp v96, v75 quad_perm:[1,0,3,2] row_mask:0xf bank_mask:0xf
	v_mov_b32_dpp v97, v74 quad_perm:[1,0,3,2] row_mask:0xf bank_mask:0xf
	v_cndmask_b32_e32 v77, v97, v81, vcc
	v_cndmask_b32_e32 v76, v96, v80, vcc
	v_cndmask_b32_e32 v75, v95, v79, vcc
	v_cndmask_b32_e32 v74, v94, v78, vcc
	v_cndmask_b32_e32 v81, v91, v97, vcc
	v_cndmask_b32_e32 v80, v90, v96, vcc
	v_lshl_add_u64 v[90:91], v[102:103], 0, v[108:109]
	v_cndmask_b32_e32 v79, v93, v95, vcc
	v_cndmask_b32_e32 v78, v92, v94, vcc
	global_store_dwordx4 v[90:91], v[74:77], off offset:128
	v_pk_fma_f32 v[70:71], v[70:71], s[2:3], v[130:131] op_sel_hi:[1,0,1]
	s_nop 0
	v_pk_fma_f32 v[64:65], v[64:65], s[2:3], v[190:191] op_sel_hi:[1,0,1]
	v_lshl_add_u64 v[74:75], v[102:103], 0, v[106:107]
	global_store_dwordx4 v[74:75], v[78:81], off offset:128
	v_pk_fma_f32 v[74:75], v[68:69], s[2:3], v[136:137] op_sel_hi:[1,0,1]
	v_pk_fma_f32 v[76:77], v[66:67], s[2:3], v[134:135] op_sel_hi:[1,0,1]
	v_cndmask_b32_e32 v66, v73, v75, vcc
	v_cndmask_b32_e32 v67, v72, v74, vcc
	v_cndmask_b32_e32 v68, v71, v77, vcc
	v_cndmask_b32_e32 v69, v70, v76, vcc
	v_mov_b32_e32 v78, v1
	v_mov_b32_e32 v79, v1
	v_mov_b32_e32 v80, v1
	v_mov_b32_e32 v81, v1
	v_mov_b32_dpp v78, v69 quad_perm:[1,0,3,2] row_mask:0xf bank_mask:0xf
	v_mov_b32_dpp v79, v68 quad_perm:[1,0,3,2] row_mask:0xf bank_mask:0xf
	v_mov_b32_dpp v80, v67 quad_perm:[1,0,3,2] row_mask:0xf bank_mask:0xf
	v_mov_b32_dpp v81, v66 quad_perm:[1,0,3,2] row_mask:0xf bank_mask:0xf
	v_cndmask_b32_e32 v69, v81, v73, vcc
	v_cndmask_b32_e32 v68, v80, v72, vcc
	v_cndmask_b32_e32 v67, v79, v71, vcc
	v_cndmask_b32_e32 v66, v78, v70, vcc
	v_cndmask_b32_e32 v73, v75, v81, vcc
	v_cndmask_b32_e32 v72, v74, v80, vcc
	v_lshl_add_u64 v[74:75], v[102:103], 0, v[100:101]
	v_cndmask_b32_e32 v71, v77, v79, vcc
	v_cndmask_b32_e32 v70, v76, v78, vcc
	global_store_dwordx4 v[74:75], v[66:69], off offset:128
	v_pk_fma_f32 v[62:63], v[62:63], s[2:3], v[188:189] op_sel_hi:[1,0,1]
	v_mov_b32_e32 v74, v1
	v_lshl_add_u64 v[66:67], v[102:103], 0, v[98:99]
	global_store_dwordx4 v[66:67], v[70:73], off offset:128
	v_add_u32_e32 v66, 0x80, v156
	v_or_b32_e32 v68, v0, v66
	v_pk_fma_f32 v[70:71], v[60:61], s[2:3], v[186:187] op_sel_hi:[1,0,1]
	v_pk_fma_f32 v[72:73], v[58:59], s[2:3], v[184:185] op_sel_hi:[1,0,1]
	v_ashrrev_i32_e32 v69, 31, v68
	v_cndmask_b32_e32 v58, v65, v71, vcc
	v_cndmask_b32_e32 v59, v64, v70, vcc
	v_cndmask_b32_e32 v60, v63, v73, vcc
	v_cndmask_b32_e32 v61, v62, v72, vcc
	v_mov_b32_e32 v67, v1
	v_mov_b32_e32 v75, v1
	v_mov_b32_e32 v76, v1
	v_lshl_add_u64 v[68:69], v[68:69], 2, s[0:1]
	v_mov_b32_dpp v67, v61 quad_perm:[1,0,3,2] row_mask:0xf bank_mask:0xf
	v_mov_b32_dpp v74, v60 quad_perm:[1,0,3,2] row_mask:0xf bank_mask:0xf
	v_mov_b32_dpp v75, v59 quad_perm:[1,0,3,2] row_mask:0xf bank_mask:0xf
	v_mov_b32_dpp v76, v58 quad_perm:[1,0,3,2] row_mask:0xf bank_mask:0xf
	v_cndmask_b32_e32 v61, v76, v65, vcc
	v_cndmask_b32_e32 v60, v75, v64, vcc
	v_cndmask_b32_e32 v59, v74, v63, vcc
	v_cndmask_b32_e32 v58, v67, v62, vcc
	v_cndmask_b32_e32 v65, v71, v76, vcc
	v_cndmask_b32_e32 v64, v70, v75, vcc
	v_lshl_add_u64 v[70:71], v[68:69], 0, v[154:155]
	v_cndmask_b32_e32 v63, v73, v74, vcc
	v_cndmask_b32_e32 v62, v72, v67, vcc
	global_store_dwordx4 v[70:71], v[58:61], off
	v_pk_fma_f32 v[70:71], v[50:51], s[2:3], v[184:185] op_sel_hi:[1,0,1]
	v_mov_b32_e32 v72, v1
	v_lshl_add_u64 v[58:59], v[68:69], 0, v[152:153]
	global_store_dwordx4 v[58:59], v[62:65], off
	v_pk_fma_f32 v[58:59], v[56:57], s[2:3], v[190:191] op_sel_hi:[1,0,1]
	v_mov_b32_e32 v73, v1
	v_pk_fma_f32 v[62:63], v[54:55], s[2:3], v[188:189] op_sel_hi:[1,0,1]
	v_pk_fma_f32 v[64:65], v[52:53], s[2:3], v[186:187] op_sel_hi:[1,0,1]
	v_cndmask_b32_e32 v54, v62, v70, vcc
	s_nop 0
	v_cndmask_b32_e32 v67, v63, v71, vcc
	v_mov_b32_dpp v72, v54 quad_perm:[1,0,3,2] row_mask:0xf bank_mask:0xf
	s_nop 0
	v_cndmask_b32_e32 v60, v59, v65, vcc
	v_cndmask_b32_e32 v61, v58, v64, vcc
	v_mov_b32_dpp v73, v67 quad_perm:[1,0,3,2] row_mask:0xf bank_mask:0xf
	v_mov_b32_e32 v67, v1
	v_mov_b32_e32 v74, v1
	v_pk_fma_f32 v[48:49], v[48:49], s[2:3], v[190:191] op_sel_hi:[1,0,1]
	v_mov_b32_dpp v67, v61 quad_perm:[1,0,3,2] row_mask:0xf bank_mask:0xf
	v_mov_b32_dpp v74, v60 quad_perm:[1,0,3,2] row_mask:0xf bank_mask:0xf
	v_cndmask_b32_e32 v61, v74, v59, vcc
	v_cndmask_b32_e32 v60, v67, v58, vcc
	v_cndmask_b32_e32 v59, v73, v63, vcc
	v_cndmask_b32_e32 v58, v72, v62, vcc
	v_cndmask_b32_e32 v63, v71, v73, vcc
	v_cndmask_b32_e32 v62, v70, v72, vcc
	v_lshl_add_u64 v[70:71], v[68:69], 0, v[148:149]
	v_cndmask_b32_e32 v65, v65, v74, vcc
	v_cndmask_b32_e32 v64, v64, v67, vcc
	global_store_dwordx4 v[70:71], v[58:61], off
	v_pk_fma_f32 v[46:47], v[46:47], s[2:3], v[188:189] op_sel_hi:[1,0,1]
	v_pk_fma_f32 v[40:41], v[40:41], s[2:3], v[190:191] op_sel_hi:[1,0,1]
	v_lshl_add_u64 v[58:59], v[68:69], 0, v[146:147]
	global_store_dwordx4 v[58:59], v[62:65], off
	v_pk_fma_f32 v[58:59], v[44:45], s[2:3], v[186:187] op_sel_hi:[1,0,1]
	v_pk_fma_f32 v[60:61], v[42:43], s[2:3], v[184:185] op_sel_hi:[1,0,1]
	v_cndmask_b32_e32 v42, v49, v59, vcc
	v_cndmask_b32_e32 v43, v48, v58, vcc
	v_cndmask_b32_e32 v44, v47, v61, vcc
	v_cndmask_b32_e32 v45, v46, v60, vcc
	v_mov_b32_e32 v62, v1
	v_mov_b32_e32 v63, v1
	v_mov_b32_e32 v64, v1
	v_mov_b32_e32 v65, v1
	v_mov_b32_dpp v62, v45 quad_perm:[1,0,3,2] row_mask:0xf bank_mask:0xf
	v_mov_b32_dpp v63, v44 quad_perm:[1,0,3,2] row_mask:0xf bank_mask:0xf
	v_mov_b32_dpp v64, v43 quad_perm:[1,0,3,2] row_mask:0xf bank_mask:0xf
	v_mov_b32_dpp v65, v42 quad_perm:[1,0,3,2] row_mask:0xf bank_mask:0xf
	v_cndmask_b32_e32 v45, v65, v49, vcc
	v_cndmask_b32_e32 v44, v64, v48, vcc
	v_cndmask_b32_e32 v43, v63, v47, vcc
	v_cndmask_b32_e32 v42, v62, v46, vcc
	v_cndmask_b32_e32 v49, v59, v65, vcc
	v_cndmask_b32_e32 v48, v58, v64, vcc
	v_lshl_add_u64 v[58:59], v[68:69], 0, v[108:109]
	v_cndmask_b32_e32 v47, v61, v63, vcc
	v_cndmask_b32_e32 v46, v60, v62, vcc
	global_store_dwordx4 v[58:59], v[42:45], off
	v_pk_fma_f32 v[38:39], v[38:39], s[2:3], v[188:189] op_sel_hi:[1,0,1]
	v_ashrrev_i32_e32 v67, 31, v66
	v_lshl_add_u64 v[42:43], v[68:69], 0, v[106:107]
	global_store_dwordx4 v[42:43], v[46:49], off
	v_pk_fma_f32 v[42:43], v[32:33], s[2:3], v[186:187] op_sel_hi:[1,0,1]
	v_pk_fma_f32 v[44:45], v[30:31], s[2:3], v[184:185] op_sel_hi:[1,0,1]
	v_cndmask_b32_e32 v30, v41, v43, vcc
	v_cndmask_b32_e32 v31, v40, v42, vcc
	v_cndmask_b32_e32 v32, v39, v45, vcc
	v_cndmask_b32_e32 v33, v38, v44, vcc
	v_mov_b32_e32 v46, v1
	v_mov_b32_e32 v47, v1
	v_mov_b32_e32 v48, v1
	v_mov_b32_e32 v49, v1
	v_mov_b32_dpp v46, v33 quad_perm:[1,0,3,2] row_mask:0xf bank_mask:0xf
	v_mov_b32_dpp v47, v32 quad_perm:[1,0,3,2] row_mask:0xf bank_mask:0xf
	v_mov_b32_dpp v48, v31 quad_perm:[1,0,3,2] row_mask:0xf bank_mask:0xf
	v_mov_b32_dpp v49, v30 quad_perm:[1,0,3,2] row_mask:0xf bank_mask:0xf
	v_cndmask_b32_e32 v33, v49, v41, vcc
	v_cndmask_b32_e32 v32, v48, v40, vcc
	v_cndmask_b32_e32 v31, v47, v39, vcc
	v_cndmask_b32_e32 v30, v46, v38, vcc
	v_cndmask_b32_e32 v41, v43, v49, vcc
	v_cndmask_b32_e32 v40, v42, v48, vcc
	v_lshl_add_u64 v[42:43], v[68:69], 0, v[100:101]
	v_cndmask_b32_e32 v39, v45, v47, vcc
	v_cndmask_b32_e32 v38, v44, v46, vcc
	global_store_dwordx4 v[42:43], v[30:33], off
	v_mov_b32_e32 v42, v1
	v_mov_b32_e32 v43, v1
	v_lshl_add_u64 v[30:31], v[68:69], 0, v[98:99]
	global_store_dwordx4 v[30:31], v[38:41], off
	v_lshl_add_u64 v[30:31], v[0:1], 0, v[66:67]
	s_nop 0
	v_pk_fma_f32 v[32:33], v[34:35], s[2:3], v[192:193] op_sel_hi:[1,0,1]
	v_lshl_add_u64 v[38:39], v[30:31], 2, s[0:1]
	v_pk_fma_f32 v[30:31], v[36:37], s[2:3], v[194:195] op_sel_hi:[1,0,1]
	v_pk_fma_f32 v[34:35], v[28:29], s[2:3], v[198:199] op_sel_hi:[1,0,1]
	v_pk_fma_f32 v[36:37], v[26:27], s[2:3], v[196:197] op_sel_hi:[1,0,1]
	v_cndmask_b32_e32 v0, v31, v35, vcc
	v_cndmask_b32_e32 v26, v30, v34, vcc
	v_cndmask_b32_e32 v27, v33, v37, vcc
	v_cndmask_b32_e32 v28, v32, v36, vcc
	v_mov_b32_e32 v40, v1
	v_mov_b32_e32 v41, v1
	v_mov_b32_dpp v42, v26 quad_perm:[1,0,3,2] row_mask:0xf bank_mask:0xf
	v_mov_b32_dpp v40, v28 quad_perm:[1,0,3,2] row_mask:0xf bank_mask:0xf
	v_mov_b32_dpp v41, v27 quad_perm:[1,0,3,2] row_mask:0xf bank_mask:0xf
	v_mov_b32_dpp v43, v0 quad_perm:[1,0,3,2] row_mask:0xf bank_mask:0xf
	v_cndmask_b32_e32 v29, v43, v31, vcc
	v_cndmask_b32_e32 v28, v42, v30, vcc
	v_cndmask_b32_e32 v27, v41, v33, vcc
	v_cndmask_b32_e32 v26, v40, v32, vcc
	v_cndmask_b32_e32 v33, v35, v43, vcc
	v_cndmask_b32_e32 v32, v34, v42, vcc
	v_lshl_add_u64 v[34:35], v[38:39], 0, v[154:155]
	v_cndmask_b32_e32 v31, v37, v41, vcc
	v_cndmask_b32_e32 v30, v36, v40, vcc
	global_store_dwordx4 v[34:35], v[26:29], off offset:128
	v_pk_fma_f32 v[24:25], v[24:25], s[2:3], v[194:195] op_sel_hi:[1,0,1]
	v_pk_fma_f32 v[22:23], v[22:23], s[2:3], v[192:193] op_sel_hi:[1,0,1]
	v_lshl_add_u64 v[26:27], v[38:39], 0, v[152:153]
	global_store_dwordx4 v[26:27], v[30:33], off offset:128
	v_pk_fma_f32 v[26:27], v[20:21], s[2:3], v[198:199] op_sel_hi:[1,0,1]
	v_pk_fma_f32 v[28:29], v[18:19], s[2:3], v[196:197] op_sel_hi:[1,0,1]
	v_cndmask_b32_e32 v0, v25, v27, vcc
	v_cndmask_b32_e32 v18, v24, v26, vcc
	v_cndmask_b32_e32 v19, v23, v29, vcc
	v_cndmask_b32_e32 v20, v22, v28, vcc
	v_mov_b32_e32 v30, v1
	v_mov_b32_e32 v31, v1
	v_mov_b32_e32 v32, v1
	v_mov_b32_e32 v33, v1
	v_mov_b32_dpp v30, v20 quad_perm:[1,0,3,2] row_mask:0xf bank_mask:0xf
	v_mov_b32_dpp v31, v19 quad_perm:[1,0,3,2] row_mask:0xf bank_mask:0xf
	v_mov_b32_dpp v32, v18 quad_perm:[1,0,3,2] row_mask:0xf bank_mask:0xf
	v_mov_b32_dpp v33, v0 quad_perm:[1,0,3,2] row_mask:0xf bank_mask:0xf
	v_cndmask_b32_e32 v21, v33, v25, vcc
	v_cndmask_b32_e32 v20, v32, v24, vcc
	v_cndmask_b32_e32 v19, v31, v23, vcc
	v_cndmask_b32_e32 v18, v30, v22, vcc
	v_cndmask_b32_e32 v25, v27, v33, vcc
	v_cndmask_b32_e32 v24, v26, v32, vcc
	v_lshl_add_u64 v[26:27], v[38:39], 0, v[148:149]
	v_cndmask_b32_e32 v23, v29, v31, vcc
	v_cndmask_b32_e32 v22, v28, v30, vcc
	global_store_dwordx4 v[26:27], v[18:21], off offset:128
	v_pk_fma_f32 v[16:17], v[16:17], s[2:3], v[194:195] op_sel_hi:[1,0,1]
	v_pk_fma_f32 v[14:15], v[14:15], s[2:3], v[192:193] op_sel_hi:[1,0,1]
	v_lshl_add_u64 v[18:19], v[38:39], 0, v[146:147]
	global_store_dwordx4 v[18:19], v[22:25], off offset:128
	v_pk_fma_f32 v[18:19], v[12:13], s[2:3], v[198:199] op_sel_hi:[1,0,1]
	v_pk_fma_f32 v[20:21], v[10:11], s[2:3], v[196:197] op_sel_hi:[1,0,1]
	v_cndmask_b32_e32 v0, v17, v19, vcc
	v_cndmask_b32_e32 v10, v16, v18, vcc
	v_cndmask_b32_e32 v11, v15, v21, vcc
	v_cndmask_b32_e32 v12, v14, v20, vcc
	v_mov_b32_e32 v22, v1
	v_mov_b32_e32 v23, v1
	v_mov_b32_e32 v24, v1
	v_mov_b32_e32 v25, v1
	v_mov_b32_dpp v22, v12 quad_perm:[1,0,3,2] row_mask:0xf bank_mask:0xf
	v_mov_b32_dpp v23, v11 quad_perm:[1,0,3,2] row_mask:0xf bank_mask:0xf
	v_mov_b32_dpp v24, v10 quad_perm:[1,0,3,2] row_mask:0xf bank_mask:0xf
	v_mov_b32_dpp v25, v0 quad_perm:[1,0,3,2] row_mask:0xf bank_mask:0xf
	v_cndmask_b32_e32 v13, v25, v17, vcc
	v_cndmask_b32_e32 v12, v24, v16, vcc
	v_cndmask_b32_e32 v11, v23, v15, vcc
	v_cndmask_b32_e32 v10, v22, v14, vcc
	v_cndmask_b32_e32 v17, v19, v25, vcc
	v_cndmask_b32_e32 v16, v18, v24, vcc
	v_lshl_add_u64 v[18:19], v[38:39], 0, v[108:109]
	v_cndmask_b32_e32 v15, v21, v23, vcc
	v_cndmask_b32_e32 v14, v20, v22, vcc
	global_store_dwordx4 v[18:19], v[10:13], off offset:128
	v_pk_fma_f32 v[8:9], v[8:9], s[2:3], v[194:195] op_sel_hi:[1,0,1]
	v_pk_fma_f32 v[6:7], v[6:7], s[2:3], v[192:193] op_sel_hi:[1,0,1]
	v_lshl_add_u64 v[10:11], v[38:39], 0, v[106:107]
	global_store_dwordx4 v[10:11], v[14:17], off offset:128
	v_pk_fma_f32 v[10:11], v[4:5], s[2:3], v[198:199] op_sel_hi:[1,0,1]
	v_pk_fma_f32 v[12:13], v[2:3], s[2:3], v[196:197] op_sel_hi:[1,0,1]
	v_cndmask_b32_e32 v0, v9, v11, vcc
	v_cndmask_b32_e32 v2, v8, v10, vcc
	v_cndmask_b32_e32 v3, v7, v13, vcc
	v_cndmask_b32_e32 v4, v6, v12, vcc
	v_mov_b32_e32 v14, v1
	v_mov_b32_e32 v15, v1
	v_mov_b32_e32 v16, v1
	v_mov_b32_dpp v14, v4 quad_perm:[1,0,3,2] row_mask:0xf bank_mask:0xf
	v_mov_b32_dpp v15, v3 quad_perm:[1,0,3,2] row_mask:0xf bank_mask:0xf
	v_mov_b32_dpp v16, v2 quad_perm:[1,0,3,2] row_mask:0xf bank_mask:0xf
	v_mov_b32_dpp v1, v0 quad_perm:[1,0,3,2] row_mask:0xf bank_mask:0xf
	v_cndmask_b32_e32 v5, v1, v9, vcc
	v_cndmask_b32_e32 v4, v16, v8, vcc
	v_cndmask_b32_e32 v3, v15, v7, vcc
	v_cndmask_b32_e32 v2, v14, v6, vcc
	v_cndmask_b32_e32 v9, v11, v1, vcc
	v_lshl_add_u64 v[0:1], v[38:39], 0, v[100:101]
	v_cndmask_b32_e32 v8, v10, v16, vcc
	v_cndmask_b32_e32 v7, v13, v15, vcc
	v_cndmask_b32_e32 v6, v12, v14, vcc
	global_store_dwordx4 v[0:1], v[2:5], off offset:128
	v_lshl_add_u64 v[0:1], v[38:39], 0, v[98:99]
	global_store_dwordx4 v[0:1], v[6:9], off offset:128
	s_endpgm
